# one static s_setprio 1 for waves 4..7 in the attention unit loop and over the mixer-prep phase (RWKV/mLSTM prep), dropped at their exits
# baseline (speedup 1.0000x reference)
; DI void attn_unit(const Args& A, LAS unsigned char* lds, int unit, int tid, int wave, int lane) {
;     const bf16* Z = (const bf16*)(A.ws + WS_Z); bf16* ao = (bf16*)(A.ws + WS_ATTO); float* al = (float*)(A.ws + WS_ATTL);
;     const int x = unit & 15; int r0 = unit >> 4; const int hh = r0 & 3; r0 >>= 2; const int b = r0 % NB, br = r0 / NB;
;     const int dil = br == 0 ? 1 : (br == 1 ? 4 : 16), lsub = SEQ / dil, nblk = lsub / 128;
;     const int res = x / nblk, nbk = x % nblk, l0 = nbk * 128, wbase = l0 - 64;
;     LAS bf16* Qs = (LAS bf16*)(lds + AT_QS); LAS bf16* Ks = (LAS bf16*)(lds + AT_KS); LAS bf16* Vt = (LAS bf16*)(lds + AT_VT); LAS float* btab = (LAS float*)(lds + AT_BT);
;     __syncthreads();
; #pragma unroll
;     for (int i = 0; i < 2; ++i) { const int id = tid + 512 * i, row = id >> 3, ch = id & 7; const int tok = b * SEQ + (l0 + row) * dil + res;
;         *(LAS u32x4_t*)(Qs + row * AT_QLD + ch * 8) = *(const u32x4_t*)(Z + (size_t)tok * ZLD + ZA + hh * 64 + ch * 8); }
;     for (int id = tid; id < 272 * 8; id += NTHR) { const int row = id >> 3, ch = id & 7; const int pos = wbase + row; u32x4_t v = (u32x4_t){0u, 0u, 0u, 0u};
;         if (row < 256 && pos >= 0 && pos < lsub) v = *(const u32x4_t*)(Z + (size_t)(b * SEQ + pos * dil + res) * ZLD + ZA + 256 + hh * 64 + ch * 8);
;         *(LAS u32x4_t*)(Ks + row * AT_QLD + ch * 8) = v; }
;     for (int id = tid; id < 272 * 8; id += NTHR) { const int key = id % 272, ch = id / 272; const int pos = wbase + key; u32x4_t v = (u32x4_t){0u, 0u, 0u, 0u};
;         if (key < 256 && pos >= 0 && pos < lsub) v = *(const u32x4_t*)(Z + (size_t)(b * SEQ + pos * dil + res) * ZLD + ZA + 512 + hh * 64 + ch * 8);
;         LAS bf16* d = Vt + (ch * 8) * AT_VLD + key;
;         d[0] = (bf16)(v.x & 0xffffu); d[AT_VLD] = (bf16)(v.x >> 16); d[2 * AT_VLD] = (bf16)(v.y & 0xffffu); d[3 * AT_VLD] = (bf16)(v.y >> 16);
;         d[4 * AT_VLD] = (bf16)(v.z & 0xffffu); d[5 * AT_VLD] = (bf16)(v.z >> 16); d[6 * AT_VLD] = (bf16)(v.w & 0xffffu); d[7 * AT_VLD] = (bf16)(v.w >> 16); }
;     if (tid < 129) btab[tid] = A.in[I_RELB][t5_bucket((tid - 64) * dil) * 4 + hh] * 1.4426950408889634f;
;     __syncthreads();
; DI void phase_attn(const Args& A, LAS unsigned char* lds, int u0, int u1, int b0, int nb, int tid, int wave, int lane) {
;     for (int u = u0 + b0; u < u1; u += nb) attn_unit(A, lds, u, tid, wave, lane);
.LBB0_244:
	s_cmp_lt_i32 s6, 4
	s_cselect_b64 s[0:1], -1, 0
	v_writelane_b32 v235, s0, 60
	s_nop 1
	v_writelane_b32 v235, s1, 61
	s_and_b64 s[0:1], s[0:1], s[2:3]
	s_andn2_b64 vcc, exec, s[0:1]
	v_writelane_b32 v235, s92, 62
	s_cbranch_vccnz .LBB0_496
	s_cmpk_gt_i32 s50, 0xa0
	s_cselect_b32 s0, 0x600, 0
	s_add_i32 s33, s0, s92
	s_cmpk_gt_i32 s33, 0x5ff
	s_mov_b32 s23, 0
	s_cbranch_scc1 .LBB0_336
	s_mov_b32 s6, s33
	s_mov_b32 s7, s50
	s_movk_i32 s8, 0x600
	v_readlane_b32 s9, v235, 52
	v_readlane_b32 s2, v235, 9
	v_readlane_b32 s3, v235, 10
	v_readlane_b32 s4, v235, 19
	v_readlane_b32 s5, v235, 20
	s_mov_b32 s72, 0x3e38aa3b
	s_mov_b32 s73, 0x3e38aa3b
	v_lshrrev_b32_e32 v2, 3, v0
	v_and_b32_e32 v3, 7, v0
	v_lshlrev_b32_e32 v3, 4, v3
	s_movk_i32 s39, 0x90
	v_mad_u32_u24 v1, v2, s39, v3
	v_and_b32_e32 v5, 0xff, v0
	v_lshrrev_b32_e32 v6, 8, v0
	s_movk_i32 s39, 0x1180
	v_mul_u32_u24_e32 v4, s39, v6
	v_lshl_add_u32 v4, v5, 1, v4
	v_add_u32_e32 v4, 0xe100, v4
	v_lshlrev_b32_e32 v6, 4, v6
	v_lshlrev_b32_e32 v8, 2, v5
	v_add_u32_e32 v8, 0x16d00, v8
	v_subrev_u32_e32 v165, 16, v0
	s_movk_i32 s39, 0x81
	v_cmp_gt_u32_e64 s[42:43], s39, v165
	s_movk_i32 s39, 0xa0
	v_cmp_gt_u32_e64 s[48:49], s39, v0
	v_cmp_gt_u32_e64 s[46:47], 64, v0
	v_cmp_gt_u32_e64 s[44:45], 16, v146
	v_subrev_u32_e32 v165, 0x50, v0
	v_cmp_lt_i32_e32 vcc, 0, v165
	v_mov_b32_e32 v7, 0
	s_nop 0
	v_cndmask_b32_e64 v166, 0, 16, vcc
	v_lshlrev_b32_e32 v167, 0, v165
	v_sub_u32_e32 v168, 0, v167
	v_max_i32_e32 v167, v167, v168
	v_cvt_f32_u32_e32 v168, v167
	v_mul_f32_e32 v168, 0x3e000000, v168
	v_max_f32_e32 v168, 1.0, v168
	v_log_f32_e32 v168, v168
	v_cmp_gt_u32_e32 vcc, 8, v167
	v_mul_f32_e32 v168, 0x3f924925, v168
	v_cvt_i32_f32_e32 v168, v168
	v_min_i32_e32 v168, 7, v168
	v_add_u32_e32 v168, 8, v168
	v_cndmask_b32_e32 v168, v168, v167, vcc
	v_add_u32_e32 v168, v168, v166
	v_lshl_or_b32 v7, v168, 0, v7
	v_lshlrev_b32_e32 v167, 2, v165
	v_sub_u32_e32 v168, 0, v167
	v_max_i32_e32 v167, v167, v168
	v_cvt_f32_u32_e32 v168, v167
	v_mul_f32_e32 v168, 0x3e000000, v168
	v_max_f32_e32 v168, 1.0, v168
	v_log_f32_e32 v168, v168
	v_cmp_gt_u32_e32 vcc, 8, v167
	v_mul_f32_e32 v168, 0x3f924925, v168
	v_cvt_i32_f32_e32 v168, v168
	v_min_i32_e32 v168, 7, v168
	v_add_u32_e32 v168, 8, v168
	v_cndmask_b32_e32 v168, v168, v167, vcc
	v_add_u32_e32 v168, v168, v166
	v_lshl_or_b32 v7, v168, 8, v7
	v_lshlrev_b32_e32 v167, 4, v165
	v_sub_u32_e32 v168, 0, v167
	v_max_i32_e32 v167, v167, v168
	v_cvt_f32_u32_e32 v168, v167
	v_mul_f32_e32 v168, 0x3e000000, v168
	v_max_f32_e32 v168, 1.0, v168
	v_log_f32_e32 v168, v168
	v_cmp_gt_u32_e32 vcc, 8, v167
	v_mul_f32_e32 v168, 0x3f924925, v168
	v_cvt_i32_f32_e32 v168, v168
	v_min_i32_e32 v168, 7, v168
	v_add_u32_e32 v168, 8, v168
	v_cndmask_b32_e32 v168, v168, v167, vcc
	v_add_u32_e32 v168, v168, v166
	v_lshl_or_b32 v7, v168, 16, v7
	v_and_b32_e32 v165, 15, v146
	v_lshrrev_b32_e32 v166, 4, v146
	s_lshl_b32 s39, s9, 4
	v_add_u32_e32 v40, s39, v165
	s_movk_i32 s40, 0x90
	v_mul_u32_u24_e32 v34, s40, v40
	v_lshl_add_u32 v34, v166, 4, v34
	v_lshlrev_b32_e32 v167, 2, v166
	v_sub_u32_e32 v35, v167, v165
	v_lshlrev_b32_e32 v35, 2, v35
	v_add_u32_e32 v35, 0x16d40, v35
	v_add_u32_e32 v167, s39, v167
	v_lshlrev_b32_e32 v36, 2, v167
	v_add_u32_e32 v36, 0x16f80, v36
	s_movk_i32 s40, 0x230
	v_mul_u32_u24_e32 v37, s40, v165
	v_lshl_add_u32 v37, v167, 1, v37
	v_add_u32_e32 v37, 0xe100, v37
	v_add_u32_e32 v9, 0x2300, v37
	v_add_u32_e32 v118, 0x4600, v37
	v_add_u32_e32 v144, 0x6900, v37
	v_xor_b32_e32 v38, 16, v146
	v_lshlrev_b32_e32 v38, 2, v38
	v_xor_b32_e32 v39, 32, v146
	v_lshlrev_b32_e32 v39, 2, v39
	v_lshlrev_b32_e32 v41, 3, v166
	v_mov_b32_e32 v232, 0
	v_mov_b32_e32 v233, 0
	s_movk_i32 s40, 0x230
	v_mul_u32_u24_e32 v168, s40, v0
	v_add_u32_e32 v168, 0xe300, v168
	s_and_saveexec_b64 s[40:41], s[46:47]
	ds_write_b64 v168, v[232:233] offset:0
	ds_write_b64 v168, v[232:233] offset:8
	ds_write_b64 v168, v[232:233] offset:16
	ds_write_b64 v168, v[232:233] offset:24
	s_mov_b64 exec, s[40:41]
	s_cmp_lt_u32 s9, 4
	s_cbranch_scc1 .LatA_prio
	s_setprio 1
.LatA_prio:
	s_and_b32 s39, s6, 15
	s_bfe_u32 s40, s6, 0x20004
	s_bfe_u32 s41, s6, 0x30006
	s_lshr_b32 s74, s6, 9
	s_lshl_b32 s75, s74, 1
	s_lshl_b32 s16, 1536, s75
	s_add_i32 s20, s75, 9
	s_add_i32 s26, s75, 4
	s_lshl_b32 s28, s74, 3
	s_lshr_b32 s29, 0x800, s75
	s_add_i32 s17, s29, -1
	s_sub_i32 s76, 4, s75
	s_lshr_b32 s77, s39, s76
	s_lshr_b32 s78, 16, s75
	s_add_i32 s78, s78, -1
	s_and_b32 s78, s39, s78
	s_lshl_b32 s19, s78, 7
	s_add_i32 s18, s19, 0xffffffc0
	s_lshl_b32 s79, s41, 11
	s_add_i32 s79, s79, s77
	s_lshl_b32 s80, s40, 7
	s_lshl_b32 s27, s40, 2
	s_mul_i32 s81, s79, 1536
	s_add_u32 s81, s81, s80
	s_add_u32 s81, s81, 0x28600000
	s_add_u32 s10, s2, s81
	s_addc_u32 s11, s3, 0
	s_lshl_b32 s82, s74, 14
	s_add_i32 s82, s82, s79
	s_lshl_b32 s83, s82, 9
	s_add_u32 s83, s83, s80
	s_add_u32 s83, s83, 0x34a00000
	s_add_u32 s12, s2, s83
	s_addc_u32 s13, s3, 0
	s_lshl_b32 s84, s82, 4
	s_add_u32 s84, s84, s27
	s_add_u32 s84, s84, 0x36200000
	s_add_u32 s14, s2, s84
	s_addc_u32 s15, s3, 0
	v_add_u32_e32 v165, s19, v2
	v_mad_u32_u24 v165, v165, s16, v3
	s_lshl_b32 s85, s16, 6
	global_load_dwordx4 v[120:123], v165, s[10:11]
	v_add_u32_e32 v166, s85, v165
	global_load_dwordx4 v[124:127], v166, s[10:11]
	v_add_u32_e32 v167, s18, v2
	v_med3_i32 v168, v167, 0, s17
	v_mad_u32_u24 v168, v168, s16, v3
	global_load_dwordx4 v[128:131], v168, s[10:11] offset:512
	v_add_u32_e32 v168, 64, v167
	v_med3_i32 v168, v168, 0, s17
	v_mad_u32_u24 v168, v168, s16, v3
	global_load_dwordx4 v[132:135], v168, s[10:11] offset:512
	v_add_u32_e32 v168, 0x80, v167
	v_med3_i32 v168, v168, 0, s17
	v_mad_u32_u24 v168, v168, s16, v3
	global_load_dwordx4 v[136:139], v168, s[10:11] offset:512
	v_add_u32_e32 v168, 0xc0, v167
	v_med3_i32 v168, v168, 0, s17
	v_mad_u32_u24 v168, v168, s16, v3
	global_load_dwordx4 v[140:143], v168, s[10:11] offset:512
	v_add_u32_e32 v169, s18, v5
	v_med3_i32 v169, v169, 0, s17
	v_mad_u32_u24 v169, v169, s16, v6
	global_load_dwordx4 v[148:151], v169, s[10:11] offset:1024
	global_load_dwordx4 v[152:155], v169, s[10:11] offset:1056
	global_load_dwordx4 v[156:159], v169, s[10:11] offset:1088
	global_load_dwordx4 v[160:163], v169, s[10:11] offset:1120
	v_bfe_u32 v171, v7, s28, 8
	v_lshl_add_u32 v171, v171, 4, s27
	s_mov_b64 exec, s[42:43]
	global_load_dword v164, v171, s[4:5]
	s_mov_b64 exec, -1

; #define LAS __attribute__((address_space(3)))
; #define MFMA16(a, b, c) __builtin_amdgcn_mfma_f32_16x16x32_bf16((a), (b), (c), 0, 0, 0)
; DI void attn_unit(const Args& A, LAS unsigned char* lds, int unit, int tid, int wave, int lane) {
;     ...
;     const int fr = lane & 15, qd = lane >> 4;
;     f32x4 acc[10];
;     { bf16x8_t qb[2];
; #pragma unroll
;       for (int ks = 0; ks < 2; ++ks) qb[ks] = *(const LAS bf16x8_t*)(Qs + (16 * wave + fr) * AT_QLD + ks * 32 + 8 * qd);
; #pragma unroll
;       for (int j = 0; j < 10; ++j) { acc[j] = (f32x4){0.f, 0.f, 0.f, 0.f};
;           if (j == 9) continue;
; #pragma unroll
;           for (int ks = 0; ks < 2; ++ks) { const bf16x8_t ka = *(const LAS bf16x8_t*)(Ks + (16 * (wave + j) + fr) * AT_QLD + ks * 32 + 8 * qd); acc[j] = MFMA16(ka, qb[ks], acc[j]); } } }
;     const int iq = 16 * wave + fr; float mx = -1.0e30f;
;     int dv[4];
; #pragma unroll
;     for (int r = 0; r < 4; ++r) dv[r] = 4 * qd + r - fr;
;     const int p0 = wbase + 16 * wave + 4 * qd;
; #pragma unroll
;     for (int j = 0; j < 9; ++j)
; #pragma unroll
;         for (int r = 0; r < 4; ++r) { const int t = 16 * j + dv[r]; bool valid = (unsigned)(p0 + 16 * j + r) < (unsigned)lsub;
;             if (j == 0) valid = valid && (dv[r] >= 0); if (j == 8) valid = valid && (dv[r] <= 0);
;             const int ti = (j == 0) ? (t < 0 ? 0 : t) : ((j == 8) ? (t > 128 ? 128 : t) : t);
;             const float s = valid ? acc[j][r] * (0.125f * 1.4426950408889634f) + btab[ti] : -1.0e30f; acc[j][r] = s; mx = fmaxf(mx, s); }
.LatA_nopf:
	s_waitcnt lgkmcnt(0)
	s_barrier
	ds_read_b128 v[172:175], v34
	ds_read_b128 v[176:179], v34 offset:64
	ds_read_b128 v[216:219], v34 offset:18432
	ds_read_b128 v[220:223], v34 offset:18496
	ds_read_b128 v[224:227], v34 offset:20736
	ds_read_b128 v[228:231], v34 offset:20800
	ds_read_b128 v[236:239], v34 offset:23040
	ds_read_b128 v[240:243], v34 offset:23104
	ds_read_b128 v[244:247], v34 offset:25344
	ds_read_b128 v[248:251], v34 offset:25408
	ds_read_b128 v[110:113], v34 offset:27648
	ds_read_b128 v[114:117], v34 offset:27712
	s_waitcnt lgkmcnt(8)
	v_mfma_f32_16x16x32_bf16 v[180:183], v[216:219], v[172:175], 0
	v_mfma_f32_16x16x32_bf16 v[180:183], v[220:223], v[176:179], v[180:183]
	ds_read_b128 v[216:219], v34 offset:29952
	ds_read_b128 v[220:223], v34 offset:30016
	s_waitcnt lgkmcnt(8)
	v_mfma_f32_16x16x32_bf16 v[184:187], v[224:227], v[172:175], 0
	v_mfma_f32_16x16x32_bf16 v[184:187], v[228:231], v[176:179], v[184:187]
	ds_read_b128 v[224:227], v34 offset:32256
	ds_read_b128 v[228:231], v34 offset:32320
	s_waitcnt lgkmcnt(8)
	v_mfma_f32_16x16x32_bf16 v[188:191], v[236:239], v[172:175], 0
	v_mfma_f32_16x16x32_bf16 v[188:191], v[240:243], v[176:179], v[188:191]
	ds_read_b128 v[236:239], v34 offset:34560
	ds_read_b128 v[240:243], v34 offset:34624
	s_waitcnt lgkmcnt(8)
	v_mfma_f32_16x16x32_bf16 v[192:195], v[244:247], v[172:175], 0
	v_mfma_f32_16x16x32_bf16 v[192:195], v[248:251], v[176:179], v[192:195]
	ds_read_b128 v[244:247], v34 offset:36864
	ds_read_b128 v[248:251], v34 offset:36928
	s_waitcnt lgkmcnt(8)
	v_mfma_f32_16x16x32_bf16 v[196:199], v[110:113], v[172:175], 0
	v_mfma_f32_16x16x32_bf16 v[196:199], v[114:117], v[176:179], v[196:199]
	s_waitcnt lgkmcnt(6)
	v_mfma_f32_16x16x32_bf16 v[200:203], v[216:219], v[172:175], 0
	v_mfma_f32_16x16x32_bf16 v[200:203], v[220:223], v[176:179], v[200:203]
	s_waitcnt lgkmcnt(4)
	v_mfma_f32_16x16x32_bf16 v[204:207], v[224:227], v[172:175], 0
	v_mfma_f32_16x16x32_bf16 v[204:207], v[228:231], v[176:179], v[204:207]
	s_waitcnt lgkmcnt(2)
	v_mfma_f32_16x16x32_bf16 v[208:211], v[236:239], v[172:175], 0
	v_mfma_f32_16x16x32_bf16 v[208:211], v[240:243], v[176:179], v[208:211]
	s_waitcnt lgkmcnt(0)
	v_mfma_f32_16x16x32_bf16 v[212:215], v[244:247], v[172:175], 0
	v_mfma_f32_16x16x32_bf16 v[212:215], v[248:251], v[176:179], v[212:215]
	s_nop 7
	ds_read2_b32 v[216:217], v35 offset0:0 offset1:1
	ds_read2_b32 v[218:219], v35 offset0:2 offset1:3
	ds_read_b128 v[220:223], v36 offset:0
	ds_read2_b32 v[224:225], v35 offset0:16 offset1:17
	ds_read2_b32 v[226:227], v35 offset0:18 offset1:19
	ds_read_b128 v[228:231], v36 offset:64
	ds_read2_b32 v[236:237], v35 offset0:32 offset1:33
	ds_read2_b32 v[238:239], v35 offset0:34 offset1:35
	ds_read_b128 v[240:243], v36 offset:128
	ds_read2_b32 v[244:245], v35 offset0:48 offset1:49
	ds_read2_b32 v[246:247], v35 offset0:50 offset1:51
	ds_read_b128 v[248:251], v36 offset:192
	v_mov_b32_e32 v46, 0xf149f2ca
	s_waitcnt lgkmcnt(9)
	v_pk_fma_f32 v[180:181], v[180:181], s[72:73], v[216:217]
	v_pk_fma_f32 v[182:183], v[182:183], s[72:73], v[218:219]
	v_pk_add_f32 v[180:181], v[180:181], v[220:221]
	v_pk_add_f32 v[182:183], v[182:183], v[222:223]
	v_max3_f32 v46, v46, v180, v181
	v_max3_f32 v46, v46, v182, v183
	ds_read2_b32 v[216:217], v35 offset0:64 offset1:65
	ds_read2_b32 v[218:219], v35 offset0:66 offset1:67
	ds_read_b128 v[220:223], v36 offset:256
	s_waitcnt lgkmcnt(9)
	v_pk_fma_f32 v[184:185], v[184:185], s[72:73], v[224:225]
	v_pk_fma_f32 v[186:187], v[186:187], s[72:73], v[226:227]
	v_pk_add_f32 v[184:185], v[184:185], v[228:229]
	v_pk_add_f32 v[186:187], v[186:187], v[230:231]
	v_max3_f32 v46, v46, v184, v185
	v_max3_f32 v46, v46, v186, v187
	ds_read2_b32 v[224:225], v35 offset0:80 offset1:81
	ds_read2_b32 v[226:227], v35 offset0:82 offset1:83
	ds_read_b128 v[228:231], v36 offset:320
	s_waitcnt lgkmcnt(9)
	v_pk_fma_f32 v[188:189], v[188:189], s[72:73], v[236:237]
	v_pk_fma_f32 v[190:191], v[190:191], s[72:73], v[238:239]
	v_pk_add_f32 v[188:189], v[188:189], v[240:241]
	v_pk_add_f32 v[190:191], v[190:191], v[242:243]
	v_max3_f32 v46, v46, v188, v189
	v_max3_f32 v46, v46, v190, v191
	ds_read2_b32 v[236:237], v35 offset0:96 offset1:97
	ds_read2_b32 v[238:239], v35 offset0:98 offset1:99
	ds_read_b128 v[240:243], v36 offset:384
	s_waitcnt lgkmcnt(9)
	v_pk_fma_f32 v[192:193], v[192:193], s[72:73], v[244:245]
	v_pk_fma_f32 v[194:195], v[194:195], s[72:73], v[246:247]
	v_pk_add_f32 v[192:193], v[192:193], v[248:249]
	v_pk_add_f32 v[194:195], v[194:195], v[250:251]
	v_max3_f32 v46, v46, v192, v193
	v_max3_f32 v46, v46, v194, v195
	ds_read2_b32 v[244:245], v35 offset0:112 offset1:113
	ds_read2_b32 v[246:247], v35 offset0:114 offset1:115
	ds_read_b128 v[248:251], v36 offset:448
	s_waitcnt lgkmcnt(9)
	v_pk_fma_f32 v[196:197], v[196:197], s[72:73], v[216:217]
	v_pk_fma_f32 v[198:199], v[198:199], s[72:73], v[218:219]
	v_pk_add_f32 v[196:197], v[196:197], v[220:221]
	v_pk_add_f32 v[198:199], v[198:199], v[222:223]
	v_max3_f32 v46, v46, v196, v197
	v_max3_f32 v46, v46, v198, v199
	ds_read2_b32 v[216:217], v35 offset0:128 offset1:129
	ds_read2_b32 v[218:219], v35 offset0:130 offset1:131
	ds_read_b128 v[220:223], v36 offset:512
	s_waitcnt lgkmcnt(9)
	v_pk_fma_f32 v[200:201], v[200:201], s[72:73], v[224:225]
	v_pk_fma_f32 v[202:203], v[202:203], s[72:73], v[226:227]
	v_pk_add_f32 v[200:201], v[200:201], v[228:229]
	v_pk_add_f32 v[202:203], v[202:203], v[230:231]
	v_max3_f32 v46, v46, v200, v201
	v_max3_f32 v46, v46, v202, v203
	s_waitcnt lgkmcnt(6)
; #define LAS __attribute__((address_space(3)))
; DI unsigned cvtpk(float lo, float hi) { const f2_t v = {lo, hi}; return __builtin_bit_cast(unsigned, __builtin_convertvector(v, bf2_t)); }
; #define MFMA16(a, b, c) __builtin_amdgcn_mfma_f32_16x16x32_bf16((a), (b), (c), 0, 0, 0)
; DI void attn_unit(const Args& A, LAS unsigned char* lds, int unit, int tid, int wave, int lane) {
;     ...
;     mx = fmaxf(mx, __shfl_xor(mx, 16)); mx = fmaxf(mx, __shfl_xor(mx, 32));
;     float lsum = 0.f;
; #pragma unroll
;     for (int j = 0; j < 9; ++j)
; #pragma unroll
;         for (int r = 0; r < 4; ++r) { const float p = __builtin_amdgcn_exp2f(acc[j][r] - mx); acc[j][r] = p; lsum += p; }
;     lsum += __shfl_xor(lsum, 16); lsum += __shfl_xor(lsum, 32);
;     f32x4 oacc[4];
; #pragma unroll
;     for (int d = 0; d < 4; ++d) oacc[d] = (f32x4){0.f, 0.f, 0.f, 0.f};
; #pragma unroll
;     for (int pp = 0; pp < 5; ++pp) {
;         union { unsigned u[4]; bf16x8_t v; } pb;
;         pb.u[0] = cvtpk(acc[2 * pp][0], acc[2 * pp][1]); pb.u[1] = cvtpk(acc[2 * pp][2], acc[2 * pp][3]); pb.u[2] = cvtpk(acc[2 * pp + 1][0], acc[2 * pp + 1][1]); pb.u[3] = cvtpk(acc[2 * pp + 1][2], acc[2 * pp + 1][3]);
; #pragma unroll
;         for (int d = 0; d < 4; ++d) { const LAS bf16* vp = Vt + (16 * d + fr) * AT_VLD + 16 * (wave + 2 * pp) + 4 * qd;
;             union { bf16x4_t h[2]; bf16x8_t v; } va; va.h[0] = *(const LAS bf16x4_t*)vp; va.h[1] = *(const LAS bf16x4_t*)(vp + 16);
;             oacc[d] = MFMA16(va.v, pb.v, oacc[d]); } }
	v_pk_fma_f32 v[204:205], v[204:205], s[72:73], v[236:237]
	v_pk_fma_f32 v[206:207], v[206:207], s[72:73], v[238:239]
	v_pk_add_f32 v[204:205], v[204:205], v[240:241]
	v_pk_add_f32 v[206:207], v[206:207], v[242:243]
	v_max3_f32 v46, v46, v204, v205
	v_max3_f32 v46, v46, v206, v207
	s_waitcnt lgkmcnt(3)
	v_pk_fma_f32 v[208:209], v[208:209], s[72:73], v[244:245]
	v_pk_fma_f32 v[210:211], v[210:211], s[72:73], v[246:247]
	v_pk_add_f32 v[208:209], v[208:209], v[248:249]
	v_pk_add_f32 v[210:211], v[210:211], v[250:251]
	v_max3_f32 v46, v46, v208, v209
	v_max3_f32 v46, v46, v210, v211
	s_waitcnt lgkmcnt(0)
	s_nop 4
	v_pk_fma_f32 v[212:213], v[212:213], s[72:73], v[216:217]
	v_pk_fma_f32 v[214:215], v[214:215], s[72:73], v[218:219]
	v_pk_add_f32 v[212:213], v[212:213], v[220:221]
	v_pk_add_f32 v[214:215], v[214:215], v[222:223]
	v_max3_f32 v46, v46, v212, v213
	v_max3_f32 v46, v46, v214, v215
	ds_bpermute_b32 v165, v38, v46
	s_waitcnt lgkmcnt(0)
	v_max_f32_e32 v46, v46, v165
	s_nop 0
	ds_bpermute_b32 v165, v39, v46
	s_waitcnt lgkmcnt(0)
	v_max_f32_e32 v46, v46, v165
	ds_read2_b64 v[216:219], v37 offset0:0 offset1:4
	ds_read2_b64 v[220:223], v9 offset0:0 offset1:4
	ds_read2_b64 v[224:227], v118 offset0:0 offset1:4
	ds_read2_b64 v[228:231], v144 offset0:0 offset1:4
	ds_read2_b64 v[236:239], v37 offset0:8 offset1:12
	ds_read2_b64 v[240:243], v9 offset0:8 offset1:12
	ds_read2_b64 v[244:247], v118 offset0:8 offset1:12
	ds_read2_b64 v[248:251], v144 offset0:8 offset1:12
	v_mov_b32_e32 v47, v46
	v_pk_add_f32 v[180:181], v[180:181], v[46:47] neg_lo:[0,1] neg_hi:[0,1]
	v_pk_add_f32 v[182:183], v[182:183], v[46:47] neg_lo:[0,1] neg_hi:[0,1]
	v_pk_add_f32 v[184:185], v[184:185], v[46:47] neg_lo:[0,1] neg_hi:[0,1]
	v_pk_add_f32 v[186:187], v[186:187], v[46:47] neg_lo:[0,1] neg_hi:[0,1]
	v_pk_add_f32 v[188:189], v[188:189], v[46:47] neg_lo:[0,1] neg_hi:[0,1]
	v_pk_add_f32 v[190:191], v[190:191], v[46:47] neg_lo:[0,1] neg_hi:[0,1]
	v_pk_add_f32 v[192:193], v[192:193], v[46:47] neg_lo:[0,1] neg_hi:[0,1]
	v_pk_add_f32 v[194:195], v[194:195], v[46:47] neg_lo:[0,1] neg_hi:[0,1]
	v_pk_add_f32 v[196:197], v[196:197], v[46:47] neg_lo:[0,1] neg_hi:[0,1]
	v_pk_add_f32 v[198:199], v[198:199], v[46:47] neg_lo:[0,1] neg_hi:[0,1]
	v_pk_add_f32 v[200:201], v[200:201], v[46:47] neg_lo:[0,1] neg_hi:[0,1]
	v_pk_add_f32 v[202:203], v[202:203], v[46:47] neg_lo:[0,1] neg_hi:[0,1]
	v_pk_add_f32 v[204:205], v[204:205], v[46:47] neg_lo:[0,1] neg_hi:[0,1]
	v_pk_add_f32 v[206:207], v[206:207], v[46:47] neg_lo:[0,1] neg_hi:[0,1]
	v_pk_add_f32 v[208:209], v[208:209], v[46:47] neg_lo:[0,1] neg_hi:[0,1]
	v_pk_add_f32 v[210:211], v[210:211], v[46:47] neg_lo:[0,1] neg_hi:[0,1]
	v_pk_add_f32 v[212:213], v[212:213], v[46:47] neg_lo:[0,1] neg_hi:[0,1]
	v_pk_add_f32 v[214:215], v[214:215], v[46:47] neg_lo:[0,1] neg_hi:[0,1]
	v_exp_f32_e32 v180, v180
	v_exp_f32_e32 v181, v181
	v_exp_f32_e32 v182, v182
	v_add_f32_e32 v145, 0, v180
	v_exp_f32_e32 v183, v183
	v_add_f32_e32 v145, v181, v145
	v_exp_f32_e32 v184, v184
	v_add_f32_e32 v145, v182, v145
	v_exp_f32_e32 v185, v185
	v_add_f32_e32 v145, v183, v145
	v_exp_f32_e32 v186, v186
	v_add_f32_e32 v145, v184, v145
	v_exp_f32_e32 v187, v187
	v_add_f32_e32 v145, v185, v145
	v_exp_f32_e32 v188, v188
	v_add_f32_e32 v145, v186, v145
	v_exp_f32_e32 v189, v189
	v_add_f32_e32 v145, v187, v145
	v_exp_f32_e32 v190, v190
	v_add_f32_e32 v145, v188, v145
	v_exp_f32_e32 v191, v191
	v_add_f32_e32 v145, v189, v145
	v_exp_f32_e32 v192, v192
	v_add_f32_e32 v145, v190, v145
	v_exp_f32_e32 v193, v193
	v_add_f32_e32 v145, v191, v145
	v_exp_f32_e32 v194, v194
	v_add_f32_e32 v145, v192, v145
	v_exp_f32_e32 v195, v195
	v_add_f32_e32 v145, v193, v145
	v_exp_f32_e32 v196, v196
	v_add_f32_e32 v145, v194, v145
	v_exp_f32_e32 v197, v197
	v_add_f32_e32 v145, v195, v145
	v_exp_f32_e32 v198, v198
	v_add_f32_e32 v145, v196, v145
	v_exp_f32_e32 v199, v199
	v_add_f32_e32 v145, v197, v145
	v_exp_f32_e32 v200, v200
	v_add_f32_e32 v145, v198, v145
	v_exp_f32_e32 v201, v201
	v_add_f32_e32 v145, v199, v145
	v_exp_f32_e32 v202, v202
	v_add_f32_e32 v145, v200, v145
	v_exp_f32_e32 v203, v203
	v_add_f32_e32 v145, v201, v145
	v_exp_f32_e32 v204, v204
	v_add_f32_e32 v145, v202, v145
	v_exp_f32_e32 v205, v205
	v_add_f32_e32 v145, v203, v145
	v_exp_f32_e32 v206, v206
	v_add_f32_e32 v145, v204, v145
	v_exp_f32_e32 v207, v207
	v_add_f32_e32 v145, v205, v145
	v_exp_f32_e32 v208, v208
	v_add_f32_e32 v145, v206, v145
	v_exp_f32_e32 v209, v209
	v_add_f32_e32 v145, v207, v145
	v_exp_f32_e32 v210, v210
	v_add_f32_e32 v145, v208, v145
	v_exp_f32_e32 v211, v211
	v_add_f32_e32 v145, v209, v145
	v_exp_f32_e32 v212, v212
	v_add_f32_e32 v145, v210, v145
	v_exp_f32_e32 v213, v213
	v_add_f32_e32 v145, v211, v145
	v_exp_f32_e32 v214, v214
	v_add_f32_e32 v145, v212, v145
	v_exp_f32_e32 v215, v215
	v_add_f32_e32 v145, v213, v145
	s_nop 0
	v_add_f32_e32 v145, v214, v145
	v_add_f32_e32 v145, v215, v145
	v_cvt_pk_bf16_f32 v110, v180, v181
	v_cvt_pk_bf16_f32 v111, v182, v183
	v_cvt_pk_bf16_f32 v112, v184, v185
	v_cvt_pk_bf16_f32 v113, v186, v187
	s_nop 1
	s_waitcnt lgkmcnt(7)
	v_mfma_f32_16x16x32_bf16 v[172:175], v[216:219], v[110:113], 0
	ds_read2_b64 v[216:219], v37 offset0:16 offset1:20
	s_waitcnt lgkmcnt(7)
	v_mfma_f32_16x16x32_bf16 v[176:179], v[220:223], v[110:113], 0
	ds_read2_b64 v[220:223], v9 offset0:16 offset1:20
	s_waitcnt lgkmcnt(7)
; #define LAS __attribute__((address_space(3)))
; DI unsigned cvtpk(float lo, float hi) { const f2_t v = {lo, hi}; return __builtin_bit_cast(unsigned, __builtin_convertvector(v, bf2_t)); }
; #define MFMA16(a, b, c) __builtin_amdgcn_mfma_f32_16x16x32_bf16((a), (b), (c), 0, 0, 0)
; DI void attn_unit(const Args& A, LAS unsigned char* lds, int unit, int tid, int wave, int lane) {
;     ...
;     f32x4 oacc[4];
; #pragma unroll
;     for (int d = 0; d < 4; ++d) oacc[d] = (f32x4){0.f, 0.f, 0.f, 0.f};
; #pragma unroll
;     for (int pp = 0; pp < 5; ++pp) {
;         union { unsigned u[4]; bf16x8_t v; } pb;
;         pb.u[0] = cvtpk(acc[2 * pp][0], acc[2 * pp][1]); pb.u[1] = cvtpk(acc[2 * pp][2], acc[2 * pp][3]); pb.u[2] = cvtpk(acc[2 * pp + 1][0], acc[2 * pp + 1][1]); pb.u[3] = cvtpk(acc[2 * pp + 1][2], acc[2 * pp + 1][3]);
; #pragma unroll
;         for (int d = 0; d < 4; ++d) { const LAS bf16* vp = Vt + (16 * d + fr) * AT_VLD + 16 * (wave + 2 * pp) + 4 * qd;
;             union { bf16x4_t h[2]; bf16x8_t v; } va; va.h[0] = *(const LAS bf16x4_t*)vp; va.h[1] = *(const LAS bf16x4_t*)(vp + 16);
;             oacc[d] = MFMA16(va.v, pb.v, oacc[d]); } }
;     const float inv = 1.f / lsum; const int tok = b * SEQ + (l0 + iq) * dil + res;
;     bf16* op = ao + ((size_t)br * NT + tok) * AW + hh * 64 + 4 * qd;
; #pragma unroll
;     for (int d = 0; d < 4; ++d) { uint2 w; w.x = cvtpk(oacc[d][0] * inv, oacc[d][1] * inv); w.y = cvtpk(oacc[d][2] * inv, oacc[d][3] * inv); *(uint2*)(op + 16 * d) = w; }
;     if (qd == 0) al[((size_t)br * NT + tok) * 4 + hh] = mx * 0.6931471805599453f + logf(lsum);
	v_mfma_f32_16x16x32_bf16 v[114:117], v[224:227], v[110:113], 0
	ds_read2_b64 v[224:227], v118 offset0:16 offset1:20
	s_waitcnt lgkmcnt(7)
	v_mfma_f32_16x16x32_bf16 v[252:255], v[228:231], v[110:113], 0
	ds_read2_b64 v[228:231], v144 offset0:16 offset1:20
	v_cvt_pk_bf16_f32 v42, v188, v189
	v_cvt_pk_bf16_f32 v43, v190, v191
	v_cvt_pk_bf16_f32 v44, v192, v193
	v_cvt_pk_bf16_f32 v45, v194, v195
	s_nop 1
	s_waitcnt lgkmcnt(7)
	v_mfma_f32_16x16x32_bf16 v[172:175], v[236:239], v[42:45], v[172:175]
	ds_read2_b64 v[236:239], v37 offset0:24 offset1:28
	s_waitcnt lgkmcnt(7)
	v_mfma_f32_16x16x32_bf16 v[176:179], v[240:243], v[42:45], v[176:179]
	ds_read2_b64 v[240:243], v9 offset0:24 offset1:28
	s_waitcnt lgkmcnt(7)
	v_mfma_f32_16x16x32_bf16 v[114:117], v[244:247], v[42:45], v[114:117]
	ds_read2_b64 v[244:247], v118 offset0:24 offset1:28
	s_waitcnt lgkmcnt(7)
	v_mfma_f32_16x16x32_bf16 v[252:255], v[248:251], v[42:45], v[252:255]
	ds_read2_b64 v[248:251], v144 offset0:24 offset1:28
	v_cvt_pk_bf16_f32 v110, v196, v197
	v_cvt_pk_bf16_f32 v111, v198, v199
	v_cvt_pk_bf16_f32 v112, v200, v201
	v_cvt_pk_bf16_f32 v113, v202, v203
	s_nop 1
	s_waitcnt lgkmcnt(7)
	v_mfma_f32_16x16x32_bf16 v[172:175], v[216:219], v[110:113], v[172:175]
	ds_read2_b64 v[216:219], v37 offset0:32 offset1:36
	s_waitcnt lgkmcnt(7)
	v_mfma_f32_16x16x32_bf16 v[176:179], v[220:223], v[110:113], v[176:179]
	ds_read2_b64 v[220:223], v9 offset0:32 offset1:36
	s_waitcnt lgkmcnt(7)
	v_mfma_f32_16x16x32_bf16 v[114:117], v[224:227], v[110:113], v[114:117]
	ds_read2_b64 v[224:227], v118 offset0:32 offset1:36
	s_waitcnt lgkmcnt(7)
	v_mfma_f32_16x16x32_bf16 v[252:255], v[228:231], v[110:113], v[252:255]
	ds_read2_b64 v[228:231], v144 offset0:32 offset1:36
	v_cvt_pk_bf16_f32 v42, v204, v205
	v_cvt_pk_bf16_f32 v43, v206, v207
	v_cvt_pk_bf16_f32 v44, v208, v209
	v_cvt_pk_bf16_f32 v45, v210, v211
	s_nop 1
	s_waitcnt lgkmcnt(7)
	v_mfma_f32_16x16x32_bf16 v[172:175], v[236:239], v[42:45], v[172:175]
	s_waitcnt lgkmcnt(6)
	v_mfma_f32_16x16x32_bf16 v[176:179], v[240:243], v[42:45], v[176:179]
	s_waitcnt lgkmcnt(5)
	v_mfma_f32_16x16x32_bf16 v[114:117], v[244:247], v[42:45], v[114:117]
	s_waitcnt lgkmcnt(4)
	v_mfma_f32_16x16x32_bf16 v[252:255], v[248:251], v[42:45], v[252:255]
	v_cvt_pk_bf16_f32 v110, v212, v213
	v_cvt_pk_bf16_f32 v111, v214, v215
	v_mov_b32_e32 v112, 0
	v_mov_b32_e32 v113, 0
	s_nop 1
	s_waitcnt lgkmcnt(3)
	v_mfma_f32_16x16x32_bf16 v[172:175], v[216:219], v[110:113], v[172:175]
	s_waitcnt lgkmcnt(2)
	v_mfma_f32_16x16x32_bf16 v[176:179], v[220:223], v[110:113], v[176:179]
	s_waitcnt lgkmcnt(1)
	v_mfma_f32_16x16x32_bf16 v[114:117], v[224:227], v[110:113], v[114:117]
	s_waitcnt lgkmcnt(0)
	v_mfma_f32_16x16x32_bf16 v[252:255], v[228:231], v[110:113], v[252:255]
	ds_bpermute_b32 v165, v38, v145
	v_add_u32_e32 v167, s34, v40
	v_lshl_add_u32 v168, v167, s35, v41
	v_lshlrev_b32_e32 v167, s36, v167
	s_waitcnt lgkmcnt(0)
	v_add_f32_e32 v145, v145, v165
	s_nop 0
	ds_bpermute_b32 v165, v39, v145
	s_waitcnt lgkmcnt(0)
	v_add_f32_e32 v169, v145, v165
	v_div_scale_f32 v165, s[40:41], v169, v169, 1.0
	v_rcp_f32_e32 v166, v165
	s_nop 0
	v_fma_f32 v171, -v165, v166, 1.0
	v_fmac_f32_e32 v166, v171, v166
	v_div_scale_f32 v171, vcc, 1.0, v169, 1.0
	v_mul_f32_e32 v232, v171, v166
	v_fma_f32 v233, -v165, v232, v171
	v_fmac_f32_e32 v232, v233, v166
	v_fma_f32 v165, -v165, v232, v171
	s_nop 1
	v_div_fmas_f32 v165, v165, v166, v232
	v_div_fixup_f32 v165, v165, v169, 1.0
	v_mul_f32_e32 v172, v165, v172
	v_mul_f32_e32 v173, v165, v173
	v_mul_f32_e32 v174, v165, v174
	v_mul_f32_e32 v175, v165, v175
	v_cvt_pk_bf16_f32 v172, v172, v173
	v_cvt_pk_bf16_f32 v173, v174, v175
	global_store_dwordx2 v168, v[172:173], s[30:31] offset:0
	v_mul_f32_e32 v176, v165, v176
	v_mul_f32_e32 v177, v165, v177
	v_mul_f32_e32 v178, v165, v178
	v_mul_f32_e32 v179, v165, v179
	v_cvt_pk_bf16_f32 v176, v176, v177
	v_cvt_pk_bf16_f32 v177, v178, v179
	global_store_dwordx2 v168, v[176:177], s[30:31] offset:32
	v_mul_f32_e32 v114, v165, v114
	v_mul_f32_e32 v115, v165, v115
	v_mul_f32_e32 v116, v165, v116
	v_mul_f32_e32 v117, v165, v117
	v_cvt_pk_bf16_f32 v114, v114, v115
	v_cvt_pk_bf16_f32 v115, v116, v117
	global_store_dwordx2 v168, v[114:115], s[30:31] offset:64
	v_mul_f32_e32 v252, v165, v252
	v_mul_f32_e32 v253, v165, v253
	v_mul_f32_e32 v254, v165, v254
	v_mul_f32_e32 v255, v165, v255
	v_cvt_pk_bf16_f32 v252, v252, v253
	v_cvt_pk_bf16_f32 v253, v254, v255
	global_store_dwordx2 v168, v[252:253], s[30:31] offset:96
	s_mov_b32 s39, 0x800000
	v_cmp_gt_f32_e32 vcc, s39, v169
	v_mov_b32_e32 v232, 0x41b17218
	s_nop 0
	v_cndmask_b32_e64 v166, 0, 32, vcc
	v_ldexp_f32 v169, v169, v166
	v_log_f32_e32 v169, v169
	v_cndmask_b32_e32 v166, 0, v232, vcc
	s_mov_b32 s39, 0x3f317217
	v_mul_f32_e32 v171, 0x3f317217, v169
	v_fma_f32 v171, v169, s39, -v171
	v_fmac_f32_e32 v171, 0x3377d1cf, v169
	v_fmac_f32_e32 v171, 0x3f317217, v169
	s_mov_b32 s39, 0x7f800000
	v_cmp_lt_f32_e64 vcc, |v169|, s39
	s_nop 1
	v_cndmask_b32_e32 v169, v169, v171, vcc
	v_sub_f32_e32 v169, v169, v166
	v_fmac_f32_e32 v169, 0x3f317218, v46
	s_mov_b64 exec, s[44:45]
	global_store_dword v167, v169, s[32:33]
	s_mov_b64 exec, -1
	s_cmp_lt_i32 s6, s8
	s_cbranch_scc1 .LatA_loop
	s_setprio 0
	s_branch .LBB0_336
.LBB0_336:
	v_readlane_b32 s80, v235, 52
	s_cmp_lt_u32 s80, 4
	s_cbranch_scc1 .Lprio_mix0
	s_setprio 1

; DI void attn_unit(const Args& A, LAS unsigned char* lds, int unit, int tid, int wave, int lane) {
;     const bf16* Z = (const bf16*)(A.ws + WS_Z); bf16* ao = (bf16*)(A.ws + WS_ATTO); float* al = (float*)(A.ws + WS_ATTL);
;     const int x = unit & 15; int r0 = unit >> 4; const int hh = r0 & 3; r0 >>= 2; const int b = r0 % NB, br = r0 / NB;
;     const int dil = br == 0 ? 1 : (br == 1 ? 4 : 16), lsub = SEQ / dil, nblk = lsub / 128;
;     const int res = x / nblk, nbk = x % nblk, l0 = nbk * 128, wbase = l0 - 64;
;     LAS bf16* Qs = (LAS bf16*)(lds + AT_QS); LAS bf16* Ks = (LAS bf16*)(lds + AT_KS); LAS bf16* Vt = (LAS bf16*)(lds + AT_VT); LAS float* btab = (LAS float*)(lds + AT_BT);
;     __syncthreads();
; #pragma unroll
;     for (int i = 0; i < 2; ++i) { const int id = tid + 512 * i, row = id >> 3, ch = id & 7; const int tok = b * SEQ + (l0 + row) * dil + res;
;         *(LAS u32x4_t*)(Qs + row * AT_QLD + ch * 8) = *(const u32x4_t*)(Z + (size_t)tok * ZLD + ZA + hh * 64 + ch * 8); }
;     for (int id = tid; id < 272 * 8; id += NTHR) { const int row = id >> 3, ch = id & 7; const int pos = wbase + row; u32x4_t v = (u32x4_t){0u, 0u, 0u, 0u};
;         if (row < 256 && pos >= 0 && pos < lsub) v = *(const u32x4_t*)(Z + (size_t)(b * SEQ + pos * dil + res) * ZLD + ZA + 256 + hh * 64 + ch * 8);
;         *(LAS u32x4_t*)(Ks + row * AT_QLD + ch * 8) = v; }
;     for (int id = tid; id < 272 * 8; id += NTHR) { const int key = id % 272, ch = id / 272; const int pos = wbase + key; u32x4_t v = (u32x4_t){0u, 0u, 0u, 0u};
;         if (key < 256 && pos >= 0 && pos < lsub) v = *(const u32x4_t*)(Z + (size_t)(b * SEQ + pos * dil + res) * ZLD + ZA + 512 + hh * 64 + ch * 8);
;         LAS bf16* d = Vt + (ch * 8) * AT_VLD + key;
;         d[0] = (bf16)(v.x & 0xffffu); d[AT_VLD] = (bf16)(v.x >> 16); d[2 * AT_VLD] = (bf16)(v.y & 0xffffu); d[3 * AT_VLD] = (bf16)(v.y >> 16);
;         d[4 * AT_VLD] = (bf16)(v.z & 0xffffu); d[5 * AT_VLD] = (bf16)(v.z >> 16); d[6 * AT_VLD] = (bf16)(v.w & 0xffffu); d[7 * AT_VLD] = (bf16)(v.w >> 16); }
;     if (tid < 129) btab[tid] = A.in[I_RELB][t5_bucket((tid - 64) * dil) * 4 + hh] * 1.4426950408889634f;
;     __syncthreads();
; template <int l> DI void run_layer(const Args& A, LAS unsigned char* lds, const XcdBarrier& bar, int lo, int hi, int G, int bid, int tid, int lane, int wave, int gw, int ngw, int gtid, int nthr) {
;     ...
;     PH(3,
.LBB0_546:
	s_setprio 0
	s_cmp_lt_i32 s6, 5
	s_cselect_b64 s[94:95], -1, 0
	s_and_b64 s[0:1], s[94:95], s[0:1]
	s_andn2_b64 vcc, exec, s[0:1]
	s_cbranch_vccnz .LBB0_957
	s_cmpk_lt_i32 s50, 0xa1
	s_cselect_b64 s[0:1], -1, 0
	s_cmpk_lt_i32 s92, 0xa0
	s_cselect_b64 s[2:3], -1, 0
	s_or_b64 s[0:1], s[2:3], s[0:1]
	s_and_b64 vcc, exec, s[0:1]
	s_cbranch_vccnz .LBB0_640
	s_add_i32 s22, s92, 0xffffff60
	s_cmpk_gt_u32 s22, 0x23f
	s_cbranch_scc1 .LBB0_639
	s_mov_b32 s6, s22
	s_add_i32 s7, s50, 0xffffff60
	s_movk_i32 s8, 0x600
	s_cmpk_lg_i32 s50, 0x100
	s_cbranch_scc1 .Latmap_s22
	s_and_b32 s8, s22, 7
	s_mulk_i32 s8, 0xc0
	s_lshr_b32 s6, s22, 3
	s_add_i32 s6, s6, s8
	s_movk_i32 s7, 12
	s_addk_i32 s8, 0xc0
.Latmap_s22:
	v_readlane_b32 s9, v235, 52
	v_readlane_b32 s2, v235, 9
	v_readlane_b32 s3, v235, 10
	v_readlane_b32 s4, v235, 19
	v_readlane_b32 s5, v235, 20
	s_mov_b32 s72, 0x3e38aa3b
	s_mov_b32 s73, 0x3e38aa3b
	v_lshrrev_b32_e32 v2, 3, v0
	v_and_b32_e32 v3, 7, v0
	v_lshlrev_b32_e32 v3, 4, v3
	s_movk_i32 s39, 0x90
	v_mad_u32_u24 v1, v2, s39, v3
	v_and_b32_e32 v5, 0xff, v0
	v_lshrrev_b32_e32 v6, 8, v0
	s_movk_i32 s39, 0x1180
	v_mul_u32_u24_e32 v4, s39, v6
	v_lshl_add_u32 v4, v5, 1, v4
	v_add_u32_e32 v4, 0xe100, v4
	v_lshlrev_b32_e32 v6, 4, v6
	v_lshlrev_b32_e32 v8, 2, v5
	v_add_u32_e32 v8, 0x16d00, v8
	v_subrev_u32_e32 v165, 16, v0
	s_movk_i32 s39, 0x81
	v_cmp_gt_u32_e64 s[42:43], s39, v165
	s_movk_i32 s39, 0xa0
	v_cmp_gt_u32_e64 s[48:49], s39, v0
	v_cmp_gt_u32_e64 s[46:47], 64, v0
	v_cmp_gt_u32_e64 s[44:45], 16, v146
	v_subrev_u32_e32 v165, 0x50, v0
	v_cmp_lt_i32_e32 vcc, 0, v165
	v_mov_b32_e32 v7, 0
	s_nop 0
	v_cndmask_b32_e64 v166, 0, 16, vcc
	v_lshlrev_b32_e32 v167, 0, v165
	v_sub_u32_e32 v168, 0, v167
	v_max_i32_e32 v167, v167, v168
	v_cvt_f32_u32_e32 v168, v167
	v_mul_f32_e32 v168, 0x3e000000, v168
	v_max_f32_e32 v168, 1.0, v168
	v_log_f32_e32 v168, v168
	v_cmp_gt_u32_e32 vcc, 8, v167
	v_mul_f32_e32 v168, 0x3f924925, v168
	v_cvt_i32_f32_e32 v168, v168
	v_min_i32_e32 v168, 7, v168
	v_add_u32_e32 v168, 8, v168
	v_cndmask_b32_e32 v168, v168, v167, vcc
	v_add_u32_e32 v168, v168, v166
	v_lshl_or_b32 v7, v168, 0, v7
	v_lshlrev_b32_e32 v167, 2, v165
	v_sub_u32_e32 v168, 0, v167
	v_max_i32_e32 v167, v167, v168
	v_cvt_f32_u32_e32 v168, v167
	v_mul_f32_e32 v168, 0x3e000000, v168
	v_max_f32_e32 v168, 1.0, v168
	v_log_f32_e32 v168, v168
	v_cmp_gt_u32_e32 vcc, 8, v167
	v_mul_f32_e32 v168, 0x3f924925, v168
	v_cvt_i32_f32_e32 v168, v168
	v_min_i32_e32 v168, 7, v168
	v_add_u32_e32 v168, 8, v168
	v_cndmask_b32_e32 v168, v168, v167, vcc
	v_add_u32_e32 v168, v168, v166
	v_lshl_or_b32 v7, v168, 8, v7
	v_lshlrev_b32_e32 v167, 4, v165
	v_sub_u32_e32 v168, 0, v167
	v_max_i32_e32 v167, v167, v168
	v_cvt_f32_u32_e32 v168, v167
	v_mul_f32_e32 v168, 0x3e000000, v168
	v_max_f32_e32 v168, 1.0, v168
	v_log_f32_e32 v168, v168
	v_cmp_gt_u32_e32 vcc, 8, v167
	v_mul_f32_e32 v168, 0x3f924925, v168
	v_cvt_i32_f32_e32 v168, v168
	v_min_i32_e32 v168, 7, v168
	v_add_u32_e32 v168, 8, v168
	v_cndmask_b32_e32 v168, v168, v167, vcc
	v_add_u32_e32 v168, v168, v166
	v_lshl_or_b32 v7, v168, 16, v7
	v_and_b32_e32 v165, 15, v146
	v_lshrrev_b32_e32 v166, 4, v146
	s_lshl_b32 s39, s9, 4
	v_add_u32_e32 v40, s39, v165
	s_movk_i32 s40, 0x90
	v_mul_u32_u24_e32 v34, s40, v40
	v_lshl_add_u32 v34, v166, 4, v34
	v_lshlrev_b32_e32 v167, 2, v166
	v_sub_u32_e32 v35, v167, v165
	v_lshlrev_b32_e32 v35, 2, v35
	v_add_u32_e32 v35, 0x16d40, v35
	v_add_u32_e32 v167, s39, v167
	v_lshlrev_b32_e32 v36, 2, v167
	v_add_u32_e32 v36, 0x16f80, v36
	s_movk_i32 s40, 0x230
	v_mul_u32_u24_e32 v37, s40, v165
	v_lshl_add_u32 v37, v167, 1, v37
	v_add_u32_e32 v37, 0xe100, v37
	v_add_u32_e32 v9, 0x2300, v37
	v_add_u32_e32 v118, 0x4600, v37
	v_add_u32_e32 v144, 0x6900, v37
	v_xor_b32_e32 v38, 16, v146
	v_lshlrev_b32_e32 v38, 2, v38
	v_xor_b32_e32 v39, 32, v146
	v_lshlrev_b32_e32 v39, 2, v39
	v_lshlrev_b32_e32 v41, 3, v166
	v_mov_b32_e32 v232, 0
	v_mov_b32_e32 v233, 0
	s_movk_i32 s40, 0x230
	v_mul_u32_u24_e32 v168, s40, v0
	v_add_u32_e32 v168, 0xe300, v168
	s_and_saveexec_b64 s[40:41], s[46:47]
	ds_write_b64 v168, v[232:233] offset:0
	ds_write_b64 v168, v[232:233] offset:8
	ds_write_b64 v168, v[232:233] offset:16
	ds_write_b64 v168, v[232:233] offset:24
	s_mov_b64 exec, s[40:41]
	s_cmp_lt_u32 s9, 4
	s_cbranch_scc1 .LatB_prio
	s_setprio 1

; #define LAS __attribute__((address_space(3)))
; DI void attn_unit(const Args& A, LAS unsigned char* lds, int unit, int tid, int wave, int lane) {
;     const bf16* Z = (const bf16*)(A.ws + WS_Z); bf16* ao = (bf16*)(A.ws + WS_ATTO); float* al = (float*)(A.ws + WS_ATTL);
;     const int x = unit & 15; int r0 = unit >> 4; const int hh = r0 & 3; r0 >>= 2; const int b = r0 % NB, br = r0 / NB;
;     const int dil = br == 0 ? 1 : (br == 1 ? 4 : 16), lsub = SEQ / dil, nblk = lsub / 128;
;     const int res = x / nblk, nbk = x % nblk, l0 = nbk * 128, wbase = l0 - 64;
;     LAS bf16* Qs = (LAS bf16*)(lds + AT_QS); LAS bf16* Ks = (LAS bf16*)(lds + AT_KS); LAS bf16* Vt = (LAS bf16*)(lds + AT_VT); LAS float* btab = (LAS float*)(lds + AT_BT);
;     __syncthreads();
; #pragma unroll
;     for (int i = 0; i < 2; ++i) { const int id = tid + 512 * i, row = id >> 3, ch = id & 7; const int tok = b * SEQ + (l0 + row) * dil + res;
;         *(LAS u32x4_t*)(Qs + row * AT_QLD + ch * 8) = *(const u32x4_t*)(Z + (size_t)tok * ZLD + ZA + hh * 64 + ch * 8); }
;     for (int id = tid; id < 272 * 8; id += NTHR) { const int row = id >> 3, ch = id & 7; const int pos = wbase + row; u32x4_t v = (u32x4_t){0u, 0u, 0u, 0u};
;         if (row < 256 && pos >= 0 && pos < lsub) v = *(const u32x4_t*)(Z + (size_t)(b * SEQ + pos * dil + res) * ZLD + ZA + 256 + hh * 64 + ch * 8);
;         *(LAS u32x4_t*)(Ks + row * AT_QLD + ch * 8) = v; }
;     for (int id = tid; id < 272 * 8; id += NTHR) { const int key = id % 272, ch = id / 272; const int pos = wbase + key; u32x4_t v = (u32x4_t){0u, 0u, 0u, 0u};
;         if (key < 256 && pos >= 0 && pos < lsub) v = *(const u32x4_t*)(Z + (size_t)(b * SEQ + pos * dil + res) * ZLD + ZA + 512 + hh * 64 + ch * 8);
;         LAS bf16* d = Vt + (ch * 8) * AT_VLD + key;
;         d[0] = (bf16)(v.x & 0xffffu); d[AT_VLD] = (bf16)(v.x >> 16); d[2 * AT_VLD] = (bf16)(v.y & 0xffffu); d[3 * AT_VLD] = (bf16)(v.y >> 16);
;         d[4 * AT_VLD] = (bf16)(v.z & 0xffffu); d[5 * AT_VLD] = (bf16)(v.z >> 16); d[6 * AT_VLD] = (bf16)(v.w & 0xffffu); d[7 * AT_VLD] = (bf16)(v.w >> 16); }
;     if (tid < 129) btab[tid] = A.in[I_RELB][t5_bucket((tid - 64) * dil) * 4 + hh] * 1.4426950408889634f;
;     __syncthreads();
.LBB0_1704:
	s_cmp_lt_i32 s6, 14
	s_cselect_b64 s[0:1], -1, 0
	v_writelane_b32 v234, s0, 44
	s_nop 1
	v_writelane_b32 v234, s1, 45
	s_and_b64 s[0:1], s[0:1], s[2:3]
	s_andn2_b64 vcc, exec, s[0:1]
	s_cbranch_vccnz .LBB0_1958
	s_cmpk_gt_i32 s50, 0xa0
	s_cselect_b32 s0, 0x600, 0
	s_add_i32 s33, s0, s92
	s_cmpk_gt_i32 s33, 0x5ff
	s_mov_b32 s3, 0
	s_cbranch_scc1 .LBB0_1796
	s_mov_b32 s6, s33
	s_mov_b32 s7, s50
	s_movk_i32 s8, 0x600
	v_readlane_b32 s9, v235, 52
	v_readlane_b32 s2, v235, 9
	v_readlane_b32 s3, v235, 10
	v_readlane_b32 s4, v235, 19
	v_readlane_b32 s5, v235, 20
	s_mov_b32 s72, 0x3e38aa3b
	s_mov_b32 s73, 0x3e38aa3b
	v_lshrrev_b32_e32 v2, 3, v0
	v_and_b32_e32 v3, 7, v0
	v_lshlrev_b32_e32 v3, 4, v3
	s_movk_i32 s39, 0x90
	v_mad_u32_u24 v1, v2, s39, v3
	v_and_b32_e32 v5, 0xff, v0
	v_lshrrev_b32_e32 v6, 8, v0
	s_movk_i32 s39, 0x1180
	v_mul_u32_u24_e32 v4, s39, v6
	v_lshl_add_u32 v4, v5, 1, v4
	v_add_u32_e32 v4, 0xe100, v4
	v_lshlrev_b32_e32 v6, 4, v6
	v_lshlrev_b32_e32 v8, 2, v5
	v_add_u32_e32 v8, 0x16d00, v8
	v_subrev_u32_e32 v165, 16, v0
	s_movk_i32 s39, 0x81
	v_cmp_gt_u32_e64 s[42:43], s39, v165
	s_movk_i32 s39, 0xa0
	v_cmp_gt_u32_e64 s[48:49], s39, v0
	v_cmp_gt_u32_e64 s[46:47], 64, v0
	v_cmp_gt_u32_e64 s[44:45], 16, v146
	v_subrev_u32_e32 v165, 0x50, v0
	v_cmp_lt_i32_e32 vcc, 0, v165
	v_mov_b32_e32 v7, 0
	s_nop 0
	v_cndmask_b32_e64 v166, 0, 16, vcc
	v_lshlrev_b32_e32 v167, 0, v165
	v_sub_u32_e32 v168, 0, v167
	v_max_i32_e32 v167, v167, v168
	v_cvt_f32_u32_e32 v168, v167
	v_mul_f32_e32 v168, 0x3e000000, v168
	v_max_f32_e32 v168, 1.0, v168
	v_log_f32_e32 v168, v168
	v_cmp_gt_u32_e32 vcc, 8, v167
	v_mul_f32_e32 v168, 0x3f924925, v168
	v_cvt_i32_f32_e32 v168, v168
	v_min_i32_e32 v168, 7, v168
	v_add_u32_e32 v168, 8, v168
	v_cndmask_b32_e32 v168, v168, v167, vcc
	v_add_u32_e32 v168, v168, v166
	v_lshl_or_b32 v7, v168, 0, v7
	v_lshlrev_b32_e32 v167, 2, v165
	v_sub_u32_e32 v168, 0, v167
	v_max_i32_e32 v167, v167, v168
	v_cvt_f32_u32_e32 v168, v167
	v_mul_f32_e32 v168, 0x3e000000, v168
	v_max_f32_e32 v168, 1.0, v168
	v_log_f32_e32 v168, v168
	v_cmp_gt_u32_e32 vcc, 8, v167
	v_mul_f32_e32 v168, 0x3f924925, v168
	v_cvt_i32_f32_e32 v168, v168
	v_min_i32_e32 v168, 7, v168
	v_add_u32_e32 v168, 8, v168
	v_cndmask_b32_e32 v168, v168, v167, vcc
	v_add_u32_e32 v168, v168, v166
	v_lshl_or_b32 v7, v168, 8, v7
	v_lshlrev_b32_e32 v167, 4, v165
	v_sub_u32_e32 v168, 0, v167
	v_max_i32_e32 v167, v167, v168
	v_cvt_f32_u32_e32 v168, v167
	v_mul_f32_e32 v168, 0x3e000000, v168
	v_max_f32_e32 v168, 1.0, v168
	v_log_f32_e32 v168, v168
	v_cmp_gt_u32_e32 vcc, 8, v167
	v_mul_f32_e32 v168, 0x3f924925, v168
	v_cvt_i32_f32_e32 v168, v168
	v_min_i32_e32 v168, 7, v168
	v_add_u32_e32 v168, 8, v168
	v_cndmask_b32_e32 v168, v168, v167, vcc
	v_add_u32_e32 v168, v168, v166
	v_lshl_or_b32 v7, v168, 16, v7
	v_and_b32_e32 v165, 15, v146
	v_lshrrev_b32_e32 v166, 4, v146
	s_lshl_b32 s39, s9, 4
	v_add_u32_e32 v40, s39, v165
	s_movk_i32 s40, 0x90
	v_mul_u32_u24_e32 v34, s40, v40
	v_lshl_add_u32 v34, v166, 4, v34
	v_lshlrev_b32_e32 v167, 2, v166
	v_sub_u32_e32 v35, v167, v165
	v_lshlrev_b32_e32 v35, 2, v35
	v_add_u32_e32 v35, 0x16d40, v35
	v_add_u32_e32 v167, s39, v167
	v_lshlrev_b32_e32 v36, 2, v167
	v_add_u32_e32 v36, 0x16f80, v36
	s_movk_i32 s40, 0x230
	v_mul_u32_u24_e32 v37, s40, v165
	v_lshl_add_u32 v37, v167, 1, v37
	v_add_u32_e32 v37, 0xe100, v37
	v_add_u32_e32 v9, 0x2300, v37
	v_add_u32_e32 v118, 0x4600, v37
	v_add_u32_e32 v144, 0x6900, v37
	v_xor_b32_e32 v38, 16, v146
	v_lshlrev_b32_e32 v38, 2, v38
	v_xor_b32_e32 v39, 32, v146
	v_lshlrev_b32_e32 v39, 2, v39
	v_lshlrev_b32_e32 v41, 3, v166
	v_mov_b32_e32 v232, 0
	v_mov_b32_e32 v233, 0
	s_movk_i32 s40, 0x230
	v_mul_u32_u24_e32 v168, s40, v0
	v_add_u32_e32 v168, 0xe300, v168
	s_and_saveexec_b64 s[40:41], s[46:47]
	ds_write_b64 v168, v[232:233] offset:0
	ds_write_b64 v168, v[232:233] offset:8
	ds_write_b64 v168, v[232:233] offset:16
	ds_write_b64 v168, v[232:233] offset:24
	s_mov_b64 exec, s[40:41]
	s_cmp_lt_u32 s9, 4
	s_cbranch_scc1 .LatC_prio
	s_setprio 1

; #define PH(k, ...) do { if (IN(pb + (k))) { { __VA_ARGS__ } if ((MK_DUP >> (k)) & 1) { xcd_barrier(bar); { __VA_ARGS__ } } } SEAM(pb + (k)); } while (0)
; template <int l> DI void run_layer(const Args& A, LAS unsigned char* lds, const XcdBarrier& bar, int lo, int hi, int G, int bid, int tid, int lane, int wave, int gw, int ngw, int gtid, int nthr) {
;     ...
;     PH(3,
;           if (G > ATT_SCAN_BLK0 && bid >= ATT_SCAN_BLK0) phase_attn(A, lds, 0, ATT_UNITS - ATT_SPLIT, bid - ATT_SCAN_BLK0, G - ATT_SCAN_BLK0, tid, wave, lane);
.LBB0_2008:
	s_setprio 0
	s_cmp_lt_i32 s6, 15
	s_cselect_b64 s[24:25], -1, 0
	s_and_b64 s[0:1], s[24:25], s[0:1]
	s_andn2_b64 vcc, exec, s[0:1]
	s_cbranch_vccnz .LBB0_2420
	s_cmpk_lt_i32 s50, 0xa1
	s_cselect_b64 s[0:1], -1, 0
	s_cmpk_lt_i32 s92, 0xa0
	s_cselect_b64 s[2:3], -1, 0
	s_or_b64 s[0:1], s[2:3], s[0:1]
	s_and_b64 vcc, exec, s[0:1]
	s_cbranch_vccnz .LBB0_2102
	s_add_i32 s33, s92, 0xffffff60
	s_cmpk_gt_u32 s33, 0x23f
	s_cbranch_scc1 .LBB0_2101
	s_mov_b32 s6, s33
	s_add_i32 s7, s50, 0xffffff60
	s_movk_i32 s8, 0x600
	s_cmpk_lg_i32 s50, 0x100
	s_cbranch_scc1 .Latmap_s33
	s_and_b32 s8, s33, 7
	s_mulk_i32 s8, 0xc0
	s_lshr_b32 s6, s33, 3
	s_add_i32 s6, s6, s8
	s_movk_i32 s7, 12
	s_addk_i32 s8, 0xc0
